# speedup vs baseline: 1.0080x; 1.0080x over previous
.Lco_noin1:
	s_cmp_lt_u32 s10, 4
	s_cbranch_scc1 .Lco_nowo
	v_and_b32_e32 v0, 0xff, v98
	v_mul_u32_u24_e32 v0, 40, v0
	v_add_u32_e32 v1, 0x2800, v0
	global_load_dwordx4 v[218:221], v0, s[48:49]
	global_load_dwordx4 v[222:225], v0, s[48:49] offset:16
	global_load_dwordx2 v[226:227], v0, s[48:49] offset:32
	global_load_dwordx4 v[228:231], v1, s[48:49]
	global_load_dwordx4 v[232:235], v1, s[48:49] offset:16
	global_load_dwordx2 v[236:237], v1, s[48:49] offset:32

.Lk_283:
	s_or_b64 exec, exec, s[0:1]
	v_lshrrev_b32_e32 v4, 4, v160
	s_lshl_b32 s0, s78, 5
	v_or_b32_e32 v165, s0, v4
	v_mov_b32_e32 v4, 0x24400
	s_add_i32 s69, s33, 33
	v_lshl_or_b32 v169, v72, 2, v4
	v_mul_u32_u24_e32 v4, 10, v160
	s_cmp_gt_i32 s77, 8
	s_cselect_b64 s[18:19], -1, 0
	s_cmp_gt_i32 s77, 10
	v_lshlrev_b32_e32 v12, 2, v4
	v_mov_b32_e32 v13, 0
	v_or_b32_e32 v164, 0x100, v160
	v_cvt_f64_f32_e32 v[10:11], v5
	v_mov_b32_e32 v5, 0x10000
	s_cselect_b64 s[20:21], -1, 0
	s_cmp_gt_i32 s77, 12
	v_lshl_add_u64 v[14:15], s[48:49], 0, v[12:13]
	v_lshlrev_b32_e32 v4, 9, v70
	v_lshlrev_b32_e32 v12, 2, v70
	v_lshl_or_b32 v67, v160, 2, v5
	v_lshl_or_b32 v69, v164, 2, v5
	s_cselect_b64 s[22:23], -1, 0
	v_add3_u32 v172, v4, s3, v75
	v_lshl_add_u64 v[4:5], s[60:61], 0, v[12:13]
	s_add_i32 s24, s24, s3
	v_lshl_add_u64 v[40:41], v[4:5], 0, 64
	v_add_u32_e32 v4, s24, v75
	v_mov_b32_e32 v5, v13
	v_lshlrev_b64 v[4:5], 11, v[4:5]
	v_cmp_gt_f32_e32 vcc, 0, v161
	v_or_b32_e32 v4, v4, v12
	v_lshrrev_b32_e32 v6, 4, v164
	v_cndmask_b32_e64 v167, 0, 1.0, vcc
	v_cmp_gt_f32_e32 vcc, 0, v162
	s_mov_b64 s[10:11], 0x2800
	s_lshl_b32 s70, s68, 16
	v_lshl_add_u64 v[4:5], s[72:73], 0, v[4:5]
	v_mov_b32_e32 v12, v13
	s_mov_b32 s26, 0x3f7d73e7
	s_mov_b32 s28, 0xa37fcc69
	s_mov_b32 s34, 0x3f779b79
	s_mov_b32 s36, 0x3d064869
	v_or_b32_e32 v166, s0, v6
	v_cndmask_b32_e64 v168, 0, 1.0, vcc
	v_cmp_gt_u32_e64 s[0:1], 32, v73
	v_lshl_add_u32 v170, v73, 5, s33
	v_lshl_add_u64 v[34:35], v[14:15], 0, s[10:11]
	s_bitset1_b32 s70, 21
	v_lshlrev_b32_e32 v171, 3, v70
	v_lshl_add_u64 v[42:43], v[4:5], 0, 64
	s_mov_b64 s[38:39], 0
	v_mov_b64_e32 v[44:45], 0
	s_mov_b64 s[24:25], 0
	s_mov_b32 s27, 0x3d8414e8
	s_mov_b32 s29, 0x3fee7078
	s_mov_b32 s3, 0xf000
	s_mov_b64 s[30:31], 0x80
	s_mov_b32 s35, 0x3f7383c5
	s_mov_b32 s37, 0x3d47c3ae
	s_mov_b32 s71, 0xffff
	v_mov_b32_e32 v47, 0x3f6f7d63
	v_bfrev_b32_e32 v173, 1
	v_mov_b32_e32 v174, 0x2f0
	v_mov_b32_e32 v175, 0x26c10
	s_mov_b64 s[40:41], 0
	s_mov_b64 s[44:45], 0
	v_mov_b32_e32 v176, 0
	v_mov_b64_e32 v[36:37], 0
	v_mov_b64_e32 v[6:7], 0
	v_mov_b64_e32 v[48:49], 0
	v_mov_b64_e32 v[38:39], 0
	v_mov_b64_e32 v[4:5], 0
	v_mov_b32_e32 v177, 0
	v_mov_b64_e32 v[50:51], v[12:13]
	v_mov_b64_e32 v[56:57], v[12:13]
	v_mov_b64_e32 v[52:53], v[12:13]
	v_mov_b64_e32 v[58:59], v[12:13]
	v_mov_b32_e32 v54, v13
	v_mov_b32_e32 v55, v13
	s_and_saveexec_b64 s[82:83], s[42:43]
	ds_write2st64_b32 v67, v218, v219 offset1:8
	ds_write2st64_b32 v67, v220, v221 offset0:16 offset1:24
	ds_write2st64_b32 v67, v222, v223 offset0:32 offset1:40
	ds_write2st64_b32 v67, v224, v225 offset0:48 offset1:56
	ds_write2st64_b32 v67, v226, v227 offset0:64 offset1:72
	ds_write2st64_b32 v69, v228, v229 offset1:8
	ds_write2st64_b32 v69, v230, v231 offset0:16 offset1:24
	ds_write2st64_b32 v69, v232, v233 offset0:32 offset1:40
	ds_write2st64_b32 v69, v234, v235 offset0:48 offset1:56
	ds_write2st64_b32 v69, v236, v237 offset0:64 offset1:72
	s_mov_b64 exec, s[82:83]
	v_mul_f32_e32 v218, v9, v18
	v_mul_f32_e32 v219, v131, v19
	v_mul_f32_e32 v220, v134, v20
	v_mul_f32_e32 v221, v137, v21
	v_mul_f32_e32 v222, v140, v22
	v_mul_f32_e32 v223, v143, v23
	v_mul_f32_e32 v224, v146, v24
	v_mul_f32_e32 v225, v150, v25
	v_mul_f32_e32 v226, v121, v26
	v_mul_f32_e32 v227, v122, v27
	v_mov_b32_e32 v250, 0
	v_add_u16_e32 v208, v250, v159
	v_add_u16_e32 v209, v250, v158
	v_add_u16_e32 v210, v250, v157
	v_add_u16_e32 v211, v250, v156
	v_add_u16_e32 v212, v250, v155
	v_add_u16_e32 v213, v250, v154
	v_add_u16_e32 v214, v250, v153
	v_add_u16_e32 v215, v250, v149
	v_add_u16_e32 v216, v250, v128
	v_add_u16_e32 v217, v250, v127
	s_mov_b64 s[86:87], 0
	s_and_saveexec_b64 s[82:83], s[42:43]
	v_lshlrev_b32_e32 v208, 2, v165
	v_lshlrev_b32_e32 v210, 2, v166
	v_add_u32_e32 v208, 0x400000, v208
	v_add_u32_e32 v210, 0x400000, v210
	v_mov_b32_e32 v209, 0x8000
	v_mov_b32_e32 v211, 0x8000
	s_mov_b64 exec, s[82:83]
	s_branch .Lk_288

.Lmy_rx:
	v_and_b32_e32 v212, 3, v177
	v_mad_u32_u24 v213, v212, v209, v208
	v_mad_u32_u24 v214, v212, v211, v210
	global_load_dword v182, v213, s[66:67] sc1
	global_load_dword v183, v214, s[66:67] sc1
	v_cmp_eq_u32_e64 s[10:11], 0, v177
	v_cmp_ne_u32_e32 vcc, 0, v177
	s_and_saveexec_b64 s[12:13], vcc
	s_cbranch_execz .Lk_291
	v_mul_f32_e32 v60, v161, v59
	v_fma_f32 v46, v167, v52, 1.0
	v_mov_b32_e32 v61, v53
	v_pk_mul_f32 v[52:53], v[60:61], v[46:47]
	v_add_u32_e32 v12, -1, v177
	v_pk_fma_f32 v[52:53], v[58:59], s[26:27], v[52:53]
	v_cvt_f64_f32_e32 v[58:59], v59
	v_fmac_f64_e32 v[58:59], s[28:29], v[44:45]
	v_cvt_f64_f32_e32 v[44:45], v57
	v_mul_f32_e32 v62, v162, v57
	v_fma_f32 v50, v168, v50, 1.0
	v_mov_b32_e32 v63, v51
	v_mov_b32_e32 v51, v47
	v_fmac_f64_e32 v[44:45], s[28:29], v[48:49]
	v_cmp_eq_u32_e32 vcc, s33, v12
	v_pk_mul_f32 v[50:51], v[62:63], v[50:51]
	v_mov_b64_e32 v[48:49], v[44:45]
	v_cndmask_b32_e32 v39, v39, v45, vcc
	v_cndmask_b32_e32 v38, v38, v44, vcc
	v_cndmask_b32_e32 v37, v37, v59, vcc
	v_cndmask_b32_e32 v36, v36, v58, vcc
	v_cmp_eq_u32_e32 vcc, s69, v177
	v_pk_fma_f32 v[50:51], v[56:57], s[26:27], v[50:51]
	s_nop 0
	v_cndmask_b32_e32 v5, v5, v45, vcc
	v_cndmask_b32_e32 v4, v4, v44, vcc
	v_cndmask_b32_e32 v7, v7, v59, vcc
	v_cndmask_b32_e32 v6, v6, v58, vcc
	v_mov_b64_e32 v[44:45], v[58:59]
.Lk_291:
	s_or_b64 exec, exec, s[12:13]
	v_add_f32_e32 v216, 1.0, v52
	v_add_f32_e32 v217, 1.0, v50
	v_lshlrev_b32_e32 v215, 9, v177
	v_cmp_neq_f32_e32 vcc, 0, v216
	v_and_b32_e32 v215, 0x1e00, v215
	v_or_b32_e32 v250, v215, v160
	v_cndmask_b32_e32 v216, v173, v216, vcc
	v_cmp_neq_f32_e32 vcc, 0, v217
	v_or_b32_e32 v251, v215, v164
	v_lshlrev_b32_e32 v250, 3, v250
	v_cndmask_b32_e32 v217, v173, v217, vcc
	v_lshlrev_b32_e32 v251, 3, v251
	s_waitcnt vmcnt(0)
	v_mov_b32_e32 v64, v182
	v_mov_b32_e32 v46, v183
	s_xor_b64 s[50:51], s[44:45], -1
	v_add_u32_e32 v12, 1, v177
	s_mov_b64 s[12:13], -1
	s_and_saveexec_b64 s[48:49], s[50:51]
	s_cbranch_execz .Lk_303
	v_lshrrev_b32_e32 v65, 20, v64
	v_cmp_eq_u32_e32 vcc, v65, v12
	v_lshrrev_b32_e32 v65, 20, v46
	v_cmp_eq_u32_e64 s[12:13], v65, v12
	s_and_b64 s[12:13], vcc, s[12:13]
	s_nop 0
	v_cndmask_b32_e64 v65, 0, 1, s[12:13]
	v_cmp_ne_u32_e32 vcc, 0, v65
	s_cmp_eq_u64 vcc, exec
	s_mov_b64 s[12:13], 0
	s_cbranch_scc1 .Lk_302
	v_lshlrev_b32_e32 v72, 13, v177
	v_and_b32_e32 v72, 0x6000, v72
	v_add_u32_e32 v65, v72, v166
	v_add_u32_e32 v72, v72, v165
	v_mov_b32_e32 v73, 0
	v_lshlrev_b64 v[56:57], 7, v[72:73]
	v_mov_b32_e32 v72, v65
	v_lshl_add_u64 v[56:57], s[66:67], 0, v[56:57]
	v_lshlrev_b64 v[60:61], 7, v[72:73]
	v_mov_b32_e32 v72, v213
	v_lshl_add_u64 v[60:61], s[66:67], 0, v[60:61]
	v_lshl_add_u64 v[58:59], s[66:67], 0, v[72:73]
	v_mov_b32_e32 v72, v214
	s_nop 0
	v_lshl_add_u64 v[62:63], s[66:67], 0, v[72:73]
	s_cmp_eq_u64 s[10:11], 0
	s_cselect_b32 s89, 0xff, 3
	s_mov_b32 s60, 0
